# attention phases: static s_setprio 1 for waves 4-7 (reset to 0 at phase end)
# speedup vs baseline: 1.0148x; 1.0038x over previous
.LBB0_544:
	s_cmp_gt_i32 s36, 6
	s_cselect_b64 s[0:1], -1, 0
	s_cmp_lt_i32 s37, 7
	s_cselect_b64 s[2:3], -1, 0
	v_writelane_b32 v255, s80, 2
	s_or_b64 s[0:1], s[0:1], s[2:3]
	v_writelane_b32 v255, s81, 3
	s_and_b64 vcc, exec, s[0:1]
	v_writelane_b32 v255, s82, 4
	s_cbranch_vccnz .LBB0_895
	v_mbcnt_hi_u32_b32 v193, -1, v253
	s_and_b32 s0, s81, 0xffffffc0
	v_add_u32_e32 v184, s0, v193
	s_cmp_gt_u32 s81, 0xff
	s_cbranch_scc0 .Lnoprio_a0
	s_setprio 1
.Lnoprio_a0:
	s_mov_b32 s46, s15
	s_mov_b64 s[6:7], s[34:35]
	s_mov_b32 s41, s14
	s_add_i32 s0, 0, 0x20468
	s_add_u32 s8, s6, 0x58000
	v_mov_b32_e32 v0, s0
	s_addc_u32 s9, s7, 0
	s_add_i32 s0, 0, 0x204a0
	s_waitcnt lgkmcnt(0)
	v_mov_b32_e32 v2, s0
	s_add_i32 s0, 0, 0x20488
	s_waitcnt vmcnt(0)
	v_mov_b32_e32 v4, s0
	ds_read_b64 v[0:1], v0
	ds_read_b64 v[2:3], v2
	ds_read_b64 v[4:5], v4
	v_readfirstlane_b32 s47, v184
	s_cmpk_lt_i32 s41, 0x110
	s_cselect_b64 s[12:13], -1, 0
	s_and_b32 s0, s47, 0xffffffc0
	s_mov_b32 s16, 0
	s_waitcnt lgkmcnt(2)
	v_readfirstlane_b32 s10, v0
	v_readfirstlane_b32 s11, v1
	s_waitcnt lgkmcnt(1)
	v_readfirstlane_b32 s48, v2
	v_readfirstlane_b32 s49, v3
	s_waitcnt lgkmcnt(0)
	v_readfirstlane_b32 s38, v4
	v_readfirstlane_b32 s39, v5
	s_cmpk_gt_i32 s41, 0x10f
	v_add_u32_e32 v200, s0, v193
	s_cbranch_scc1 .LBB0_598
	s_add_u32 s50, s6, 0x4619c000
	s_addc_u32 s51, s7, 0
	s_add_u32 s52, s6, 0x49d1c000
	s_addc_u32 s53, s7, 0
	s_add_u32 s54, s6, 0x216b8000
	s_addc_u32 s55, s7, 0
	s_add_u32 s56, s6, 0x37e0c000
	s_addc_u32 s57, s7, 0
	s_movk_i32 s58, 0xff
	s_movk_i32 s59, 0x100
	s_movk_i32 s60, 0x2000
	s_movk_i32 s61, 0xc00
	v_mov_b32_e32 v187, 0
	v_mov_b32_e32 v185, 0x358637bd
	s_mov_b32 s62, 0x800000
	s_mov_b32 s63, 0x2aaaaaab
	s_movk_i32 s64, 0x600
	s_movk_i32 s65, 0xd0
	s_movk_i32 s66, 0x50
	s_add_i32 s67, 0, 0x10000
	s_mov_b32 s68, 0xaaaaaaab
	s_mov_b32 s69, 0xc3e00000
	v_mov_b32_e32 v201, 0x7149f2ca
	s_mov_b32 s40, 0x3dd53b94
	s_mov_b32 s70, 0x41000000
	v_mov_b32_e32 v202, 0xc0a00000
	v_mov_b32_e32 v203, 0x43e00000
	v_mov_b32_e32 v204, 0xf149f2ca
	s_mov_b32 s71, s41
	s_branch .LBB0_548

.LBB0_845:
	s_setprio 0
	s_cmp_lt_u32 s37, 8
	s_cbranch_scc1 .LBB0_895
	s_waitcnt vmcnt(0)
	v_or_b32_e32 v0, s82, v193
	v_cmp_eq_u32_e32 vcc, 0, v0
	s_barrier
	s_and_saveexec_b64 s[0:1], vcc
	s_cbranch_execz .LBB0_894
	v_mov_b32_e32 v0, s80
	s_waitcnt vmcnt(0) expcnt(0) lgkmcnt(0)
	ds_read_b32 v2, v0
	ds_read_b32 v0, v0 offset:4
	s_waitcnt lgkmcnt(1)
	v_cmp_ne_u32_e32 vcc, 0, v2
	s_cbranch_vccnz .LBB0_862
	v_readlane_b32 s2, v255, 0
	v_readlane_b32 s3, v255, 1
	s_load_dwordx2 s[6:7], s[2:3], 0x4
	s_add_u32 s2, s34, 0x1000
	s_addc_u32 s3, s35, 0
	s_add_u32 s4, s34, 0x1100
	s_addc_u32 s5, s35, 0
	s_waitcnt lgkmcnt(0)
	s_mul_i32 s18, s6, s15
	s_add_u32 s6, s34, 0x1200
	s_mul_i32 s18, s18, s7
	s_addc_u32 s7, s35, 0
	s_add_u32 s8, s34, 0x1300
	s_addc_u32 s9, s35, 0
	s_mov_b32 s19, 1
	v_mov_b32_e32 v16, 0
	s_branch .LBB0_850

.LBB0_1859:
	s_cmp_gt_i32 s36, 19
	s_cselect_b64 s[0:1], -1, 0
	s_cmp_lt_i32 s37, 20
	s_cselect_b64 s[2:3], -1, 0
	s_or_b64 s[0:1], s[0:1], s[2:3]
	s_and_b64 vcc, exec, s[0:1]
	s_cbranch_vccnz .LBB0_2175
	v_mbcnt_hi_u32_b32 v195, -1, v253
	s_and_b32 s0, s81, 0xffffffc0
	s_cmp_gt_u32 s81, 0xff
	s_cbranch_scc0 .Lnoprio_a1
	s_setprio 1
.Lnoprio_a1:
	v_add_u32_e32 v184, s0, v195
	s_mov_b64 s[6:7], s[34:35]
	s_mov_b32 s44, s14
	s_mov_b32 s42, s15
	s_add_i32 s0, 0, 0x20468
	s_add_u32 s8, s6, 0x58000
	v_mov_b32_e32 v0, s0
	s_addc_u32 s9, s7, 0
	s_add_i32 s0, 0, 0x204a0
	s_waitcnt lgkmcnt(0)
	v_mov_b32_e32 v2, s0
	s_add_i32 s0, 0, 0x20488
	s_waitcnt vmcnt(0)
	v_mov_b32_e32 v4, s0
	ds_read_b64 v[0:1], v0
	ds_read_b64 v[2:3], v2
	ds_read_b64 v[4:5], v4
	v_readfirstlane_b32 s45, v184
	s_cmpk_lt_i32 s44, 0x100
	s_cselect_b64 s[12:13], -1, 0
	s_and_b32 s0, s45, 0xffffffc0
	s_mov_b32 s16, 0
	s_waitcnt lgkmcnt(2)
	v_readfirstlane_b32 s10, v0
	v_readfirstlane_b32 s11, v1
	s_waitcnt lgkmcnt(1)
	v_readfirstlane_b32 s46, v2
	v_readfirstlane_b32 s47, v3
	s_waitcnt lgkmcnt(0)
	v_readfirstlane_b32 s39, v4
	v_readfirstlane_b32 s43, v5
	s_movk_i32 s48, 0x100
	s_movk_i32 s49, 0xff
	s_cmpk_gt_i32 s44, 0xff
	v_add_u32_e32 v202, s0, v195
	s_cbranch_scc1 .LBB0_1899
	s_add_u32 s50, s6, 0x4619c000
	s_addc_u32 s51, s7, 0
	s_add_u32 s52, s6, 0x49d1c000
	s_addc_u32 s53, s7, 0
	s_add_u32 s54, s6, 0x216b8000
	s_addc_u32 s55, s7, 0
	s_add_u32 s56, s6, 0x37e0c000
	s_addc_u32 s57, s7, 0
	s_movk_i32 s58, 0xc00
	v_mov_b32_e32 v187, 0
	s_movk_i32 s59, 0x2000
	v_mov_b32_e32 v185, 0x358637bd
	s_mov_b32 s60, 0x800000
	s_mov_b32 s61, 0x2aaaaaab
	s_movk_i32 s62, 0x600
	s_movk_i32 s63, 0xd0
	s_movk_i32 s64, 0x50
	s_add_i32 s65, 0, 0x10000
	s_mov_b32 s66, 0xaaaaaaab
	s_mov_b32 s67, 0xc3e00000
	v_mov_b32_e32 v203, 0x7149f2ca
	s_mov_b32 s38, 0x3dd53b94
	s_mov_b32 s68, 0x41000000
	v_mov_b32_e32 v204, 0xc0a00000
	v_mov_b32_e32 v205, 0x43e00000
	v_mov_b32_e32 v206, 0xf149f2ca
	s_mov_b32 s69, s44
	s_branch .LBB0_1863

.LBB0_2123:
	s_lshl_b32 s12, s63, 7
	v_cmp_gt_u32_e32 vcc, 32, v167
	s_and_saveexec_b64 s[10:11], vcc
	s_cbranch_execz .LBB0_2014
	v_lshl_add_u32 v0, v166, 2, s65
	ds_write_b32 v0, v80
	s_branch .LBB0_2014
	s_setprio 0
